# v30 + every run of consecutive s_nop merged into the fewest s_nop with the same wait states
# baseline (speedup 1.0000x reference)
.LBB0_146:
	s_or_b64 exec, exec, s[72:73]
	v_lshl_add_u64 v[70:71], v[78:79], 0, s[66:67]
	s_waitcnt lgkmcnt(0)
	v_mfma_f32_16x16x32_bf16 v[78:81], v[6:9], v[66:69], 0
	s_add_i32 s70, s96, s70
	s_cmpk_lt_i32 s70, 0x100
	v_lshl_add_u64 v[76:77], v[76:77], 0, s[24:25]
	s_nop 4
	v_add_f32_e32 v78, v10, v78
	v_mul_f32_e64 v82, |v78|, s35
	v_exp_f32_e32 v89, v82
	v_add_f32_e32 v83, v11, v79
	v_min_f32_e32 v82, 0, v78
	v_mul_f32_e64 v78, |v83|, s35
	v_exp_f32_e32 v116, v78
	v_add_f32_e32 v80, v12, v80
	v_min_f32_e32 v83, 0, v83
	v_add_f32_e32 v81, v13, v81
	s_nop 15
	s_nop 0
	v_mul_f32_e64 v92, |v80|, s35
	v_exp_f32_e32 v118, v92
	v_min_f32_e32 v80, 0, v80
	s_nop 12
	v_add_f32_e32 v91, 1.0, v116
	v_log_f32_e32 v91, v91
	s_nop 1
	v_mul_f32_e32 v91, 0x3f317218, v91
	s_nop 5
	v_add_f32_e32 v90, 1.0, v89
	v_log_f32_e32 v90, v90
	s_nop 1
	v_mul_f32_e32 v90, 0x3f317218, v90
	s_nop 1
	v_pk_add_f32 v[90:91], v[82:83], v[90:91] neg_lo:[0,1] neg_hi:[0,1]
	v_mul_f32_e64 v82, |v81|, s35
	v_exp_f32_e32 v119, v82
	v_min_f32_e32 v81, 0, v81
	s_nop 15
	s_nop 2
	v_lshl_add_u64 v[94:95], s[2:3], 2, v[70:71]
	s_nop 14
	v_add_f32_e32 v83, 1.0, v119
	v_log_f32_e32 v83, v83
	s_nop 1
	v_mul_f32_e32 v83, 0x3f317218, v83
	s_nop 5
	v_add_f32_e32 v82, 1.0, v118
	v_log_f32_e32 v82, v82
	s_nop 1
	v_mul_f32_e32 v82, 0x3f317218, v82
	s_nop 1
	v_pk_add_f32 v[80:81], v[80:81], v[82:83] neg_lo:[0,1] neg_hi:[0,1]
	s_nop 0
	v_pk_mul_f32 v[82:83], v[80:81], s[44:45] op_sel_hi:[1,0]
	v_pk_mul_f32 v[80:81], v[90:91], s[44:45] op_sel_hi:[1,0]
	v_mfma_f32_16x16x32_bf16 v[90:93], v[2:5], v[66:69], 0
	global_store_dwordx4 v[94:95], v[80:83], off
	s_nop 6
	v_add_f32_e32 v89, v14, v90
	v_mul_f32_e64 v90, |v89|, s35
	v_exp_f32_e32 v118, v90
	v_min_f32_e32 v80, 0, v89
	v_add_f32_e32 v81, v15, v91
	v_mul_f32_e64 v82, |v81|, s35
	v_exp_f32_e32 v119, v82
	v_min_f32_e32 v81, 0, v81
	s_nop 1
	v_add_f32_e32 v89, v16, v92
	s_nop 15
	s_nop 0
	v_mul_f32_e64 v90, |v89|, s35
	s_nop 13
	v_add_f32_e32 v83, 1.0, v119
	v_log_f32_e32 v83, v83
	s_nop 1
	v_mul_f32_e32 v83, 0x3f317218, v83
	s_nop 1
	v_exp_f32_e32 v119, v90
	s_nop 3
	v_add_f32_e32 v82, 1.0, v118
	v_log_f32_e32 v82, v82
	s_nop 1
	v_mul_f32_e32 v82, 0x3f317218, v82
	s_nop 1
	v_pk_add_f32 v[80:81], v[80:81], v[82:83] neg_lo:[0,1] neg_hi:[0,1]
	v_min_f32_e32 v82, 0, v89
	v_add_f32_e32 v83, v17, v93
	v_mul_f32_e64 v90, |v83|, s35
	v_exp_f32_e32 v118, v90
	v_min_f32_e32 v83, 0, v83
	v_pk_mul_f32 v[80:81], v[80:81], s[44:45] op_sel_hi:[1,0]
	s_nop 15
	s_nop 1
	v_lshl_add_u64 v[94:95], s[10:11], 2, v[70:71]
	s_nop 14
	v_add_f32_e32 v91, 1.0, v118
	v_log_f32_e32 v91, v91
	s_nop 1
	v_mul_f32_e32 v91, 0x3f317218, v91
	s_nop 5
	v_add_f32_e32 v90, 1.0, v119
	v_log_f32_e32 v90, v90
	s_nop 1
	v_mul_f32_e32 v90, 0x3f317218, v90
	s_nop 1
	v_pk_add_f32 v[82:83], v[82:83], v[90:91] neg_lo:[0,1] neg_hi:[0,1]
	v_mfma_f32_16x16x32_bf16 v[90:93], v[22:25], v[66:69], 0
	v_mul_f32_e64 v82, v82, s44
	v_mul_f32_e64 v83, v83, s44
	global_store_dwordx4 v[94:95], v[80:83], off
	s_nop 4
	v_add_f32_e32 v89, v26, v90
	v_mul_f32_e64 v90, |v89|, s35
	v_exp_f32_e32 v118, v90
	v_min_f32_e32 v80, 0, v89
	v_add_f32_e32 v81, v27, v91
	v_mul_f32_e64 v82, |v81|, s35
	v_exp_f32_e32 v119, v82
	v_min_f32_e32 v81, 0, v81
	s_nop 1
	v_add_f32_e32 v89, v28, v92
	s_nop 15
	s_nop 0
	v_mul_f32_e64 v90, |v89|, s35
	s_nop 13
	v_add_f32_e32 v83, 1.0, v119
	v_log_f32_e32 v83, v83
	s_nop 1
	v_mul_f32_e32 v83, 0x3f317218, v83
	s_nop 1
	v_exp_f32_e32 v119, v90
	s_nop 3
	v_add_f32_e32 v82, 1.0, v118
	v_log_f32_e32 v82, v82
	s_nop 1
	v_mul_f32_e32 v82, 0x3f317218, v82
	s_nop 1
	v_pk_add_f32 v[80:81], v[80:81], v[82:83] neg_lo:[0,1] neg_hi:[0,1]
	v_min_f32_e32 v82, 0, v89
	v_add_f32_e32 v83, v29, v93
	v_mul_f32_e64 v90, |v83|, s35
	v_exp_f32_e32 v118, v90
	v_min_f32_e32 v83, 0, v83
	v_pk_mul_f32 v[80:81], v[80:81], s[44:45] op_sel_hi:[1,0]
	s_nop 15
	s_nop 1
	v_lshl_add_u64 v[94:95], s[12:13], 2, v[70:71]
	s_nop 14
	v_add_f32_e32 v91, 1.0, v118
	v_log_f32_e32 v91, v91
	s_nop 1
	v_mul_f32_e32 v91, 0x3f317218, v91
	s_nop 5
	v_add_f32_e32 v90, 1.0, v119
	v_log_f32_e32 v90, v90
	s_nop 1
	v_mul_f32_e32 v90, 0x3f317218, v90
	s_nop 1
	v_pk_add_f32 v[82:83], v[82:83], v[90:91] neg_lo:[0,1] neg_hi:[0,1]
	v_mfma_f32_16x16x32_bf16 v[90:93], v[18:21], v[66:69], 0
	v_mul_f32_e64 v82, v82, s44
	v_mul_f32_e64 v83, v83, s44
	global_store_dwordx4 v[94:95], v[80:83], off
	s_nop 4
	v_add_f32_e32 v89, v30, v90
	v_mul_f32_e64 v90, |v89|, s35
	v_exp_f32_e32 v118, v90
	v_min_f32_e32 v80, 0, v89
	v_add_f32_e32 v81, v31, v91
	v_mul_f32_e64 v82, |v81|, s35
	v_exp_f32_e32 v119, v82
	v_min_f32_e32 v81, 0, v81
	s_nop 1
	v_add_f32_e32 v89, v32, v92
	s_nop 15
	s_nop 0
	v_mul_f32_e64 v90, |v89|, s35
	s_nop 13
	v_add_f32_e32 v83, 1.0, v119
	v_log_f32_e32 v83, v83
	s_nop 1
	v_mul_f32_e32 v83, 0x3f317218, v83
	s_nop 1
	v_exp_f32_e32 v119, v90
	s_nop 3
	v_add_f32_e32 v82, 1.0, v118
	v_log_f32_e32 v82, v82
	s_nop 1
	v_mul_f32_e32 v82, 0x3f317218, v82
	s_nop 1
	v_pk_add_f32 v[80:81], v[80:81], v[82:83] neg_lo:[0,1] neg_hi:[0,1]
	v_min_f32_e32 v82, 0, v89
	v_add_f32_e32 v83, v33, v93
	v_mul_f32_e64 v90, |v83|, s35
	v_exp_f32_e32 v118, v90
	v_min_f32_e32 v83, 0, v83
	v_pk_mul_f32 v[80:81], v[80:81], s[44:45] op_sel_hi:[1,0]
	s_nop 15
	s_nop 1
	v_lshl_add_u64 v[94:95], s[14:15], 2, v[70:71]
	s_nop 14
	v_add_f32_e32 v91, 1.0, v118
	v_log_f32_e32 v91, v91
	s_nop 1
	v_mul_f32_e32 v91, 0x3f317218, v91
	s_nop 5
	v_add_f32_e32 v90, 1.0, v119
	v_log_f32_e32 v90, v90
	s_nop 1
	v_mul_f32_e32 v90, 0x3f317218, v90
	s_nop 1
	v_pk_add_f32 v[82:83], v[82:83], v[90:91] neg_lo:[0,1] neg_hi:[0,1]
	v_mfma_f32_16x16x32_bf16 v[90:93], v[38:41], v[66:69], 0
	v_mul_f32_e64 v82, v82, s44
	v_mul_f32_e64 v83, v83, s44
	global_store_dwordx4 v[94:95], v[80:83], off
	s_nop 4
	v_add_f32_e32 v89, v42, v90
	v_mul_f32_e64 v90, |v89|, s35
	v_exp_f32_e32 v118, v90
	v_min_f32_e32 v80, 0, v89
	v_add_f32_e32 v81, v43, v91
	v_mul_f32_e64 v82, |v81|, s35
	v_exp_f32_e32 v119, v82
	v_min_f32_e32 v81, 0, v81
	s_nop 1
	v_add_f32_e32 v89, v44, v92
	s_nop 15
	s_nop 0
	v_mul_f32_e64 v90, |v89|, s35
	s_nop 13
	v_add_f32_e32 v83, 1.0, v119
	v_log_f32_e32 v83, v83
	s_nop 1
	v_mul_f32_e32 v83, 0x3f317218, v83
	s_nop 1
	v_exp_f32_e32 v119, v90
	s_nop 3
	v_add_f32_e32 v82, 1.0, v118
	v_log_f32_e32 v82, v82
	s_nop 1
	v_mul_f32_e32 v82, 0x3f317218, v82
	s_nop 1
	v_pk_add_f32 v[80:81], v[80:81], v[82:83] neg_lo:[0,1] neg_hi:[0,1]
	v_min_f32_e32 v82, 0, v89
	v_add_f32_e32 v83, v45, v93
	v_mul_f32_e64 v90, |v83|, s35
	v_exp_f32_e32 v118, v90
	v_min_f32_e32 v83, 0, v83
	v_pk_mul_f32 v[80:81], v[80:81], s[44:45] op_sel_hi:[1,0]
	s_nop 15
	s_nop 1
	v_lshl_add_u64 v[94:95], s[16:17], 2, v[70:71]
	s_nop 14
	v_add_f32_e32 v91, 1.0, v118
	v_log_f32_e32 v91, v91
	s_nop 1
	v_mul_f32_e32 v91, 0x3f317218, v91
	s_nop 5
	v_add_f32_e32 v90, 1.0, v119
	v_log_f32_e32 v90, v90
	s_nop 1
	v_mul_f32_e32 v90, 0x3f317218, v90
	s_nop 1
	v_pk_add_f32 v[82:83], v[82:83], v[90:91] neg_lo:[0,1] neg_hi:[0,1]
	v_mfma_f32_16x16x32_bf16 v[90:93], v[34:37], v[66:69], 0
	v_mul_f32_e64 v82, v82, s44
	v_mul_f32_e64 v83, v83, s44
	global_store_dwordx4 v[94:95], v[80:83], off
	s_nop 4
	v_add_f32_e32 v89, v46, v90
	v_mul_f32_e64 v90, |v89|, s35
	v_exp_f32_e32 v118, v90
	v_min_f32_e32 v80, 0, v89
	v_add_f32_e32 v81, v47, v91
	v_mul_f32_e64 v82, |v81|, s35
	v_exp_f32_e32 v119, v82
	v_min_f32_e32 v81, 0, v81
	s_nop 1
	v_add_f32_e32 v89, v48, v92
	s_nop 15
	s_nop 0
	v_mul_f32_e64 v90, |v89|, s35
	s_nop 13
	v_add_f32_e32 v83, 1.0, v119
	v_log_f32_e32 v83, v83
	s_nop 1
	v_mul_f32_e32 v83, 0x3f317218, v83
	s_nop 1
	v_exp_f32_e32 v119, v90
	s_nop 3
	v_add_f32_e32 v82, 1.0, v118
	v_log_f32_e32 v82, v82
	s_nop 1
	v_mul_f32_e32 v82, 0x3f317218, v82
	s_nop 1
	v_pk_add_f32 v[80:81], v[80:81], v[82:83] neg_lo:[0,1] neg_hi:[0,1]
	v_min_f32_e32 v82, 0, v89
	v_add_f32_e32 v83, v49, v93
	v_mul_f32_e64 v90, |v83|, s35
	v_exp_f32_e32 v118, v90
	v_min_f32_e32 v83, 0, v83
	v_pk_mul_f32 v[80:81], v[80:81], s[44:45] op_sel_hi:[1,0]
	s_nop 15
	s_nop 1
	v_lshl_add_u64 v[94:95], s[18:19], 2, v[70:71]
	s_nop 14
	v_add_f32_e32 v91, 1.0, v118
	v_log_f32_e32 v91, v91
	s_nop 1
	v_mul_f32_e32 v91, 0x3f317218, v91
	s_nop 5
	v_add_f32_e32 v90, 1.0, v119
	v_log_f32_e32 v90, v90
	s_nop 1
	v_mul_f32_e32 v90, 0x3f317218, v90
	s_nop 1
	v_pk_add_f32 v[82:83], v[82:83], v[90:91] neg_lo:[0,1] neg_hi:[0,1]
	v_mfma_f32_16x16x32_bf16 v[90:93], v[54:57], v[66:69], 0
	v_mul_f32_e64 v82, v82, s44
	v_mul_f32_e64 v83, v83, s44
	global_store_dwordx4 v[94:95], v[80:83], off
	v_mfma_f32_16x16x32_bf16 v[66:69], v[50:53], v[66:69], 0
	s_nop 3
	v_add_f32_e32 v89, v58, v90
	v_mul_f32_e64 v90, |v89|, s35
	v_exp_f32_e32 v118, v90
	v_min_f32_e32 v80, 0, v89
	v_add_f32_e32 v66, v62, v66
	v_add_f32_e32 v67, v63, v67
	v_add_f32_e32 v81, v59, v91
	v_mul_f32_e64 v82, |v81|, s35
	v_exp_f32_e32 v119, v82
	v_min_f32_e32 v81, 0, v81
	v_add_f32_e32 v68, v64, v68
	v_add_f32_e32 v69, v65, v69
	v_add_f32_e32 v89, v60, v92
	s_nop 15
	s_nop 0
	v_mul_f32_e64 v90, |v89|, s35
	s_nop 13
	v_add_f32_e32 v83, 1.0, v119
	v_log_f32_e32 v83, v83
	s_nop 1
	v_mul_f32_e32 v83, 0x3f317218, v83
	s_nop 1
	v_exp_f32_e32 v119, v90
	s_nop 3
	v_add_f32_e32 v82, 1.0, v118
	v_log_f32_e32 v82, v82
	s_nop 1
	v_mul_f32_e32 v82, 0x3f317218, v82
	s_nop 1
	v_pk_add_f32 v[80:81], v[80:81], v[82:83] neg_lo:[0,1] neg_hi:[0,1]
	v_min_f32_e32 v82, 0, v89
	v_add_f32_e32 v83, v61, v93
	v_mul_f32_e64 v90, |v83|, s35
	v_exp_f32_e32 v118, v90
	v_min_f32_e32 v83, 0, v83
	v_pk_mul_f32 v[80:81], v[80:81], s[44:45] op_sel_hi:[1,0]
	s_nop 15
	s_nop 15
	s_nop 1
	v_add_f32_e32 v91, 1.0, v118
	v_log_f32_e32 v91, v91
	s_nop 1
	v_mul_f32_e32 v91, 0x3f317218, v91
	s_nop 5
	v_add_f32_e32 v90, 1.0, v119
	v_log_f32_e32 v90, v90
	s_nop 1
	v_mul_f32_e32 v90, 0x3f317218, v90
	s_nop 1
	v_mul_f32_e64 v89, |v66|, s35
	v_exp_f32_e32 v89, v89
	v_pk_add_f32 v[82:83], v[82:83], v[90:91] neg_lo:[0,1] neg_hi:[0,1]
	v_lshl_add_u64 v[90:91], s[20:21], 2, v[70:71]
	v_pk_mul_f32 v[82:83], v[82:83], s[44:45] op_sel_hi:[1,0]
	global_store_dwordx4 v[90:91], v[80:83], off
	v_min_f32_e32 v66, 0, v66
	v_lshl_add_u64 v[70:71], s[22:23], 2, v[70:71]
	v_mul_f32_e64 v80, |v67|, s35
	v_exp_f32_e32 v114, v80
	v_min_f32_e32 v67, 0, v67
	s_nop 15
	s_nop 3
	v_mul_f32_e64 v82, |v68|, s35
	v_min_f32_e32 v68, 0, v68
	s_nop 12
	v_add_f32_e32 v81, 1.0, v114
	v_log_f32_e32 v81, v81
	s_nop 1
	v_mul_f32_e32 v81, 0x3f317218, v81
	s_nop 1
	v_exp_f32_e32 v114, v82
	s_nop 2
	v_add_f32_e32 v80, 1.0, v89
	v_log_f32_e32 v80, v80
	s_nop 1
	v_mul_f32_e32 v80, 0x3f317218, v80
	s_nop 1
	v_pk_add_f32 v[66:67], v[66:67], v[80:81] neg_lo:[0,1] neg_hi:[0,1]
	v_mul_f32_e64 v80, |v69|, s35
	v_exp_f32_e32 v115, v80
	v_min_f32_e32 v69, 0, v69
	v_pk_mul_f32 v[66:67], v[66:67], s[44:45] op_sel_hi:[1,0]
	s_nop 15
	s_nop 15
	s_nop 1
	v_add_f32_e32 v79, 1.0, v115
	v_log_f32_e32 v79, v79
	s_nop 1
	v_mul_f32_e32 v79, 0x3f317218, v79
	s_nop 1
	v_cmp_lt_f32_e64 vcc, |v114|, s45
	s_nop 3
	v_add_f32_e32 v78, 1.0, v114
	v_log_f32_e32 v78, v78
	s_nop 1
	v_mul_f32_e32 v78, 0x3f317218, v78
	s_nop 1
	v_pk_add_f32 v[68:69], v[68:69], v[78:79] neg_lo:[0,1] neg_hi:[0,1]
	s_nop 0
	v_pk_mul_f32 v[68:69], v[68:69], s[44:45] op_sel_hi:[1,0]
	global_store_dwordx4 v[70:71], v[66:69], off
	s_barrier
	s_cbranch_scc0 .LBB0_161

.LBB0_153:
	s_nop 0
	v_mov_b32_e32 v66, 0
	v_mov_b32_e32 v68, 0
	v_mov_b32_e32 v69, 0
	v_mov_b32_e32 v70, 0
	v_mov_b32_e32 v71, 0
	s_waitcnt lgkmcnt(0)
	s_barrier
	s_and_saveexec_b64 s[72:73], s[4:5]
	ds_read_b128 v[68:71], v72
	s_or_b64 exec, exec, s[72:73]
	s_waitcnt lgkmcnt(0)
	v_mfma_f32_16x16x32_bf16 v[80:83], v[6:9], v[68:71], 0
	s_ashr_i32 s71, s70, 31
	s_lshl_b64 s[72:73], s[70:71], 18
	v_lshl_or_b32 v78, v130, 12, s72
	s_nop 4
	v_add_f32_e32 v67, v10, v80
	v_mul_f32_e64 v79, |v67|, s35
	v_exp_f32_e32 v89, v79
	v_min_f32_e32 v90, 0, v67
	v_add_f32_e32 v82, v12, v82
	v_add_f32_e32 v83, v13, v83
	v_add_f32_e32 v91, v11, v81
	v_mul_f32_e64 v80, |v91|, s35
	v_exp_f32_e32 v118, v80
	v_min_f32_e32 v91, 0, v91
	v_mov_b32_e32 v79, s73
	v_lshl_add_u64 v[78:79], v[74:75], 0, v[78:79]
	s_nop 15
	s_nop 15
	s_nop 0
	v_add_f32_e32 v93, 1.0, v118
	v_log_f32_e32 v93, v93
	s_nop 1
	v_mul_f32_e32 v93, 0x3f317218, v93
	s_nop 1
	v_mul_f32_e64 v92, |v82|, s35
	v_exp_f32_e32 v120, v92
	v_min_f32_e32 v82, 0, v82
	s_nop 2
	v_add_f32_e32 v92, 1.0, v89
	v_log_f32_e32 v92, v92
	s_nop 1
	v_mul_f32_e32 v92, 0x3f317218, v92
	s_nop 1
	v_pk_add_f32 v[90:91], v[90:91], v[92:93] neg_lo:[0,1] neg_hi:[0,1]
	v_mul_f32_e64 v92, |v83|, s35
	v_exp_f32_e32 v121, v92
	v_min_f32_e32 v83, 0, v83
	v_pk_mul_f32 v[90:91], v[90:91], s[44:45] op_sel_hi:[1,0]
	s_nop 15
	s_nop 2
	v_mfma_f32_16x16x32_bf16 v[94:97], v[2:5], v[68:71], 0
	s_nop 13
	v_add_f32_e32 v93, 1.0, v121
	v_log_f32_e32 v93, v93
	s_nop 1
	v_mul_f32_e32 v93, 0x3f317218, v93
	s_nop 5
	v_add_f32_e32 v92, 1.0, v120
	v_log_f32_e32 v92, v92
	s_nop 1
	v_mul_f32_e32 v92, 0x3f317218, v92
	s_nop 1
	v_pk_add_f32 v[82:83], v[82:83], v[92:93] neg_lo:[0,1] neg_hi:[0,1]
	v_add_f32_e32 v67, v14, v94
	v_pk_mul_f32 v[92:93], v[82:83], s[44:45] op_sel_hi:[1,0]
	v_mul_f32_e64 v82, |v67|, s35
	v_exp_f32_e32 v89, v82
	v_lshl_add_u64 v[82:83], s[2:3], 2, v[78:79]
	global_store_dwordx4 v[82:83], v[90:93], off
	s_nop 1
	v_min_f32_e32 v90, 0, v67
	v_add_f32_e32 v91, v15, v95
	v_mul_f32_e64 v92, |v91|, s35
	v_exp_f32_e32 v122, v92
	v_min_f32_e32 v91, 0, v91
	s_nop 15
	s_nop 3
	v_add_f32_e32 v94, v16, v96
	s_nop 13
	v_add_f32_e32 v93, 1.0, v122
	v_log_f32_e32 v93, v93
	s_nop 1
	v_mul_f32_e32 v93, 0x3f317218, v93
	s_nop 1
	v_mul_f32_e64 v92, |v94|, s35
	v_exp_f32_e32 v122, v92
	s_nop 3
	v_add_f32_e32 v92, 1.0, v89
	v_log_f32_e32 v92, v92
	s_nop 1
	v_mul_f32_e32 v92, 0x3f317218, v92
	s_nop 1
	v_pk_add_f32 v[90:91], v[90:91], v[92:93] neg_lo:[0,1] neg_hi:[0,1]
	v_add_f32_e32 v93, v17, v97
	v_min_f32_e32 v92, 0, v94
	v_mul_f32_e64 v94, |v93|, s35
	v_exp_f32_e32 v123, v94
	v_min_f32_e32 v93, 0, v93
	v_pk_mul_f32 v[90:91], v[90:91], s[44:45] op_sel_hi:[1,0]
	s_nop 15
	s_nop 15
	s_nop 1
	v_add_f32_e32 v95, 1.0, v123
	v_log_f32_e32 v95, v95
	s_nop 1
	v_mul_f32_e32 v95, 0x3f317218, v95
	s_nop 5
	v_add_f32_e32 v94, 1.0, v122
	v_log_f32_e32 v94, v94
	s_nop 1
	v_mul_f32_e32 v94, 0x3f317218, v94
	s_nop 1
	v_pk_add_f32 v[92:93], v[92:93], v[94:95] neg_lo:[0,1] neg_hi:[0,1]
	v_mfma_f32_16x16x32_bf16 v[94:97], v[22:25], v[68:71], 0
	v_mul_f32_e64 v92, v92, s44
	v_mul_f32_e64 v93, v93, s44
	global_store_dwordx4 v[82:83], v[90:93], off offset:64
	s_nop 4
	v_add_f32_e32 v67, v26, v94
	v_mul_f32_e64 v89, |v67|, s35
	v_exp_f32_e32 v89, v89
	v_min_f32_e32 v90, 0, v67
	v_add_f32_e32 v91, v27, v95
	v_mul_f32_e64 v92, |v91|, s35
	v_exp_f32_e32 v122, v92
	v_min_f32_e32 v91, 0, v91
	s_nop 15
	s_nop 3
	v_add_f32_e32 v94, v28, v96
	s_nop 13
	v_add_f32_e32 v93, 1.0, v122
	v_log_f32_e32 v93, v93
	s_nop 1
	v_mul_f32_e32 v93, 0x3f317218, v93
	s_nop 1
	v_mul_f32_e64 v92, |v94|, s35
	v_exp_f32_e32 v122, v92
	s_nop 3
	v_add_f32_e32 v92, 1.0, v89
	v_log_f32_e32 v92, v92
	s_nop 1
	v_mul_f32_e32 v92, 0x3f317218, v92
	s_nop 1
	v_pk_add_f32 v[90:91], v[90:91], v[92:93] neg_lo:[0,1] neg_hi:[0,1]
	v_add_f32_e32 v93, v29, v97
	v_min_f32_e32 v92, 0, v94
	v_mul_f32_e64 v94, |v93|, s35
	v_exp_f32_e32 v123, v94
	v_min_f32_e32 v93, 0, v93
	v_pk_mul_f32 v[90:91], v[90:91], s[44:45] op_sel_hi:[1,0]
	s_nop 15
	s_nop 15
	s_nop 1
	v_add_f32_e32 v95, 1.0, v123
	v_log_f32_e32 v95, v95
	s_nop 1
	v_mul_f32_e32 v95, 0x3f317218, v95
	s_nop 5
	v_add_f32_e32 v94, 1.0, v122
	v_log_f32_e32 v94, v94
	s_nop 1
	v_mul_f32_e32 v94, 0x3f317218, v94
	s_nop 1
	v_pk_add_f32 v[92:93], v[92:93], v[94:95] neg_lo:[0,1] neg_hi:[0,1]
	v_mfma_f32_16x16x32_bf16 v[94:97], v[18:21], v[68:71], 0
	v_mul_f32_e64 v92, v92, s44
	v_mul_f32_e64 v93, v93, s44
	global_store_dwordx4 v[82:83], v[90:93], off offset:128
	s_nop 4
	v_add_f32_e32 v67, v30, v94
	v_mul_f32_e64 v89, |v67|, s35
	v_exp_f32_e32 v89, v89
	v_min_f32_e32 v90, 0, v67
	v_add_f32_e32 v91, v31, v95
	v_mul_f32_e64 v92, |v91|, s35
	v_exp_f32_e32 v122, v92
	v_min_f32_e32 v91, 0, v91
	s_nop 15
	s_nop 3
	v_add_f32_e32 v94, v32, v96
	s_nop 13
	v_add_f32_e32 v93, 1.0, v122
	v_log_f32_e32 v93, v93
	s_nop 1
	v_mul_f32_e32 v93, 0x3f317218, v93
	s_nop 1
	v_mul_f32_e64 v92, |v94|, s35
	v_exp_f32_e32 v122, v92
	s_nop 3
	v_add_f32_e32 v92, 1.0, v89
	v_log_f32_e32 v92, v92
	s_nop 1
	v_mul_f32_e32 v92, 0x3f317218, v92
	s_nop 1
	v_pk_add_f32 v[90:91], v[90:91], v[92:93] neg_lo:[0,1] neg_hi:[0,1]
	v_add_f32_e32 v93, v33, v97
	v_min_f32_e32 v92, 0, v94
	v_mul_f32_e64 v94, |v93|, s35
	v_exp_f32_e32 v123, v94
	v_min_f32_e32 v93, 0, v93
	v_pk_mul_f32 v[90:91], v[90:91], s[44:45] op_sel_hi:[1,0]
	s_nop 15
	s_nop 15
	s_nop 1
	v_add_f32_e32 v95, 1.0, v123
	v_log_f32_e32 v95, v95
	s_nop 1
	v_mul_f32_e32 v95, 0x3f317218, v95
	s_nop 5
	v_add_f32_e32 v94, 1.0, v122
	v_log_f32_e32 v94, v94
	s_nop 1
	v_mul_f32_e32 v94, 0x3f317218, v94
	s_nop 1
	v_pk_add_f32 v[92:93], v[92:93], v[94:95] neg_lo:[0,1] neg_hi:[0,1]
	v_mfma_f32_16x16x32_bf16 v[94:97], v[38:41], v[68:71], 0
	v_mul_f32_e64 v92, v92, s44
	v_mul_f32_e64 v93, v93, s44
	global_store_dwordx4 v[82:83], v[90:93], off offset:192
	s_nop 4
	v_add_f32_e32 v67, v42, v94
	v_mul_f32_e64 v89, |v67|, s35
	v_exp_f32_e32 v89, v89
	v_min_f32_e32 v90, 0, v67
	v_add_f32_e32 v91, v43, v95
	v_mul_f32_e64 v92, |v91|, s35
	v_exp_f32_e32 v122, v92
	v_min_f32_e32 v91, 0, v91
	s_nop 15
	s_nop 3
	v_add_f32_e32 v94, v44, v96
	s_nop 13
	v_add_f32_e32 v93, 1.0, v122
	v_log_f32_e32 v93, v93
	s_nop 1
	v_mul_f32_e32 v93, 0x3f317218, v93
	s_nop 1
	v_mul_f32_e64 v92, |v94|, s35
	v_exp_f32_e32 v122, v92
	s_nop 3
	v_add_f32_e32 v92, 1.0, v89
	v_log_f32_e32 v92, v92
	s_nop 1
	v_mul_f32_e32 v92, 0x3f317218, v92
	s_nop 1
	v_pk_add_f32 v[90:91], v[90:91], v[92:93] neg_lo:[0,1] neg_hi:[0,1]
	v_add_f32_e32 v93, v45, v97
	v_min_f32_e32 v92, 0, v94
	v_mul_f32_e64 v94, |v93|, s35
	v_exp_f32_e32 v123, v94
	v_min_f32_e32 v93, 0, v93
	v_pk_mul_f32 v[90:91], v[90:91], s[44:45] op_sel_hi:[1,0]
	s_nop 15
	s_nop 15
	s_nop 1
	v_add_f32_e32 v95, 1.0, v123
	v_log_f32_e32 v95, v95
	s_nop 1
	v_mul_f32_e32 v95, 0x3f317218, v95
	s_nop 5
	v_add_f32_e32 v94, 1.0, v122
	v_log_f32_e32 v94, v94
	s_nop 1
	v_mul_f32_e32 v94, 0x3f317218, v94
	s_nop 1
	v_pk_add_f32 v[92:93], v[92:93], v[94:95] neg_lo:[0,1] neg_hi:[0,1]
	v_mfma_f32_16x16x32_bf16 v[94:97], v[34:37], v[68:71], 0
	v_mul_f32_e64 v92, v92, s44
	v_mul_f32_e64 v93, v93, s44
	global_store_dwordx4 v[82:83], v[90:93], off offset:256
	s_nop 4
	v_add_f32_e32 v67, v46, v94
	v_mul_f32_e64 v89, |v67|, s35
	v_exp_f32_e32 v89, v89
	v_min_f32_e32 v90, 0, v67
	v_add_f32_e32 v91, v47, v95
	v_mul_f32_e64 v92, |v91|, s35
	v_exp_f32_e32 v122, v92
	v_min_f32_e32 v91, 0, v91
	s_nop 15
	s_nop 3
	v_add_f32_e32 v94, v48, v96
	s_nop 13
	v_add_f32_e32 v93, 1.0, v122
	v_log_f32_e32 v93, v93
	s_nop 1
	v_mul_f32_e32 v93, 0x3f317218, v93
	s_nop 1
	v_mul_f32_e64 v92, |v94|, s35
	v_exp_f32_e32 v122, v92
	s_nop 3
	v_add_f32_e32 v92, 1.0, v89
	v_log_f32_e32 v92, v92
	s_nop 1
	v_mul_f32_e32 v92, 0x3f317218, v92
	s_nop 1
	v_pk_add_f32 v[90:91], v[90:91], v[92:93] neg_lo:[0,1] neg_hi:[0,1]
	v_add_f32_e32 v93, v49, v97
	v_min_f32_e32 v92, 0, v94
	v_mul_f32_e64 v94, |v93|, s35
	v_exp_f32_e32 v123, v94
	v_min_f32_e32 v93, 0, v93
	v_pk_mul_f32 v[90:91], v[90:91], s[44:45] op_sel_hi:[1,0]
	s_nop 15
	s_nop 15
	s_nop 1
	v_add_f32_e32 v95, 1.0, v123
	v_log_f32_e32 v95, v95
	s_nop 1
	v_mul_f32_e32 v95, 0x3f317218, v95
	s_nop 5
	v_add_f32_e32 v94, 1.0, v122
	v_log_f32_e32 v94, v94
	s_nop 1
	v_mul_f32_e32 v94, 0x3f317218, v94
	s_nop 1
	v_pk_add_f32 v[92:93], v[92:93], v[94:95] neg_lo:[0,1] neg_hi:[0,1]
	v_mfma_f32_16x16x32_bf16 v[94:97], v[54:57], v[68:71], 0
	v_mul_f32_e64 v92, v92, s44
	v_mul_f32_e64 v93, v93, s44
	global_store_dwordx4 v[82:83], v[90:93], off offset:320
	v_mfma_f32_16x16x32_bf16 v[68:71], v[50:53], v[68:71], 0
	s_nop 3
	v_add_f32_e32 v67, v58, v94
	v_mul_f32_e64 v89, |v67|, s35
	v_exp_f32_e32 v89, v89
	v_min_f32_e32 v90, 0, v67
	v_add_f32_e32 v69, v63, v69
	v_add_f32_e32 v70, v64, v70
	v_add_f32_e32 v91, v59, v95
	v_mul_f32_e64 v92, |v91|, s35
	v_exp_f32_e32 v122, v92
	v_min_f32_e32 v91, 0, v91
	v_add_f32_e32 v71, v65, v71
	s_nop 15
	s_nop 2
	v_add_f32_e32 v94, v60, v96
	s_nop 13
	v_add_f32_e32 v93, 1.0, v122
	v_log_f32_e32 v93, v93
	s_nop 1
	v_mul_f32_e32 v93, 0x3f317218, v93
	s_nop 1
	v_mul_f32_e64 v92, |v94|, s35
	v_exp_f32_e32 v122, v92
	s_nop 3
	v_add_f32_e32 v92, 1.0, v89
	v_log_f32_e32 v92, v92
	s_nop 1
	v_mul_f32_e32 v92, 0x3f317218, v92
	s_nop 1
	v_pk_add_f32 v[90:91], v[90:91], v[92:93] neg_lo:[0,1] neg_hi:[0,1]
	v_add_f32_e32 v93, v61, v97
	v_min_f32_e32 v92, 0, v94
	v_mul_f32_e64 v94, |v93|, s35
	v_exp_f32_e32 v123, v94
	v_min_f32_e32 v93, 0, v93
	v_pk_mul_f32 v[90:91], v[90:91], s[44:45] op_sel_hi:[1,0]
	s_nop 15
	s_nop 15
	s_nop 1
	v_add_f32_e32 v95, 1.0, v123
	v_log_f32_e32 v95, v95
	s_nop 1
	v_mul_f32_e32 v95, 0x3f317218, v95
	s_nop 5
	v_add_f32_e32 v94, 1.0, v122
	v_log_f32_e32 v94, v94
	s_nop 1
	v_mul_f32_e32 v94, 0x3f317218, v94
	s_nop 1
	v_add_f32_e32 v67, v62, v68
	v_mul_f32_e64 v68, |v67|, s35
	v_exp_f32_e32 v89, v68
	v_pk_add_f32 v[92:93], v[92:93], v[94:95] neg_lo:[0,1] neg_hi:[0,1]
	v_min_f32_e32 v68, 0, v67
	v_pk_mul_f32 v[92:93], v[92:93], s[44:45] op_sel_hi:[1,0]
	global_store_dwordx4 v[82:83], v[90:93], off offset:384
	s_nop 1
	v_mul_f32_e64 v90, |v69|, s35
	v_exp_f32_e32 v118, v90
	v_min_f32_e32 v69, 0, v69
	s_nop 15
	s_nop 15
	s_nop 2
	v_add_f32_e32 v91, 1.0, v118
	v_log_f32_e32 v91, v91
	s_nop 1
	v_mul_f32_e32 v91, 0x3f317218, v91
	s_nop 1
	v_mul_f32_e64 v90, |v70|, s35
	v_exp_f32_e32 v118, v90
	v_min_f32_e32 v70, 0, v70
	s_nop 2
	v_add_f32_e32 v90, 1.0, v89
	v_log_f32_e32 v90, v90
	s_nop 1
	v_mul_f32_e32 v90, 0x3f317218, v90
	s_nop 1
	v_pk_add_f32 v[68:69], v[68:69], v[90:91] neg_lo:[0,1] neg_hi:[0,1]
	v_mul_f32_e64 v90, |v71|, s35
	v_exp_f32_e32 v119, v90
	v_min_f32_e32 v71, 0, v71
	v_pk_mul_f32 v[68:69], v[68:69], s[44:45] op_sel_hi:[1,0]
	s_nop 15
	s_nop 15
	s_nop 2
	v_add_f32_e32 v81, 1.0, v119
	v_log_f32_e32 v81, v81
	s_nop 1
	v_mul_f32_e32 v81, 0x3f317218, v81
	s_nop 5
	v_add_f32_e32 v80, 1.0, v118
	v_log_f32_e32 v80, v80
	s_nop 1
	v_mul_f32_e32 v80, 0x3f317218, v80
	s_nop 1
	v_pk_add_f32 v[70:71], v[70:71], v[80:81] neg_lo:[0,1] neg_hi:[0,1]
	v_mov_b32_e32 v67, 0
	v_pk_mul_f32 v[70:71], v[70:71], s[44:45] op_sel_hi:[1,0]
	global_store_dwordx4 v[82:83], v[68:71], off offset:448
	s_nop 1
	v_mov_b32_e32 v68, 0
	v_mov_b32_e32 v69, 0
	s_and_saveexec_b64 s[72:73], s[4:5]
	ds_read_b128 v[66:69], v72 offset:512
	s_or_b64 exec, exec, s[72:73]
	s_waitcnt lgkmcnt(0)
	v_mfma_f32_16x16x32_bf16 v[80:83], v[6:9], v[66:69], 0
	v_lshl_add_u64 v[70:71], v[78:79], 0, s[62:63]
	s_nop 6
	v_add_f32_e32 v80, v10, v80
	v_mul_f32_e64 v89, |v80|, s35
	v_exp_f32_e32 v89, v89
	v_add_f32_e32 v91, v11, v81
	v_min_f32_e32 v90, 0, v80
	v_mul_f32_e64 v80, |v91|, s35
	v_exp_f32_e32 v118, v80
	v_add_f32_e32 v82, v12, v82
	v_min_f32_e32 v91, 0, v91
	v_add_f32_e32 v83, v13, v83
	s_nop 15
	s_nop 0
	v_mul_f32_e64 v94, |v82|, s35
	v_exp_f32_e32 v120, v94
	v_min_f32_e32 v82, 0, v82
	s_nop 12
	v_add_f32_e32 v93, 1.0, v118
	v_log_f32_e32 v93, v93
	s_nop 1
	v_mul_f32_e32 v93, 0x3f317218, v93
	s_nop 5
	v_add_f32_e32 v92, 1.0, v89
	v_log_f32_e32 v92, v92
	s_nop 1
	v_mul_f32_e32 v92, 0x3f317218, v92
	s_nop 1
	v_pk_add_f32 v[90:91], v[90:91], v[92:93] neg_lo:[0,1] neg_hi:[0,1]
	v_mul_f32_e64 v92, |v83|, s35
	v_exp_f32_e32 v121, v92
	v_min_f32_e32 v83, 0, v83
	v_pk_mul_f32 v[90:91], v[90:91], s[44:45] op_sel_hi:[1,0]
	s_nop 15
	s_nop 2
	v_mfma_f32_16x16x32_bf16 v[94:97], v[2:5], v[66:69], 0
	s_nop 13
	v_add_f32_e32 v93, 1.0, v121
	v_log_f32_e32 v93, v93
	s_nop 1
	v_mul_f32_e32 v93, 0x3f317218, v93
	s_nop 5
	v_add_f32_e32 v92, 1.0, v120
	v_log_f32_e32 v92, v92
	s_nop 1
	v_mul_f32_e32 v92, 0x3f317218, v92
	s_nop 1
	v_pk_add_f32 v[82:83], v[82:83], v[92:93] neg_lo:[0,1] neg_hi:[0,1]
	v_add_f32_e32 v89, v14, v94
	v_pk_mul_f32 v[92:93], v[82:83], s[44:45] op_sel_hi:[1,0]
	v_mul_f32_e64 v82, |v89|, s35
	v_exp_f32_e32 v120, v82
	v_lshl_add_u64 v[82:83], s[2:3], 2, v[70:71]
	global_store_dwordx4 v[82:83], v[90:93], off
	v_min_f32_e32 v82, 0, v89
	v_add_f32_e32 v83, v15, v95
	v_mul_f32_e64 v90, |v83|, s35
	v_exp_f32_e32 v121, v90
	v_min_f32_e32 v83, 0, v83
	s_nop 15
	s_nop 3
	v_add_f32_e32 v92, v16, v96
	s_nop 13
	v_add_f32_e32 v91, 1.0, v121
	v_log_f32_e32 v91, v91
	s_nop 1
	v_mul_f32_e32 v91, 0x3f317218, v91
	s_nop 1
	v_mul_f32_e64 v90, |v92|, s35
	v_exp_f32_e32 v121, v90
	s_nop 3
	v_add_f32_e32 v90, 1.0, v120
	v_log_f32_e32 v90, v90
	s_nop 1
	v_mul_f32_e32 v90, 0x3f317218, v90
	s_nop 1
	v_pk_add_f32 v[82:83], v[82:83], v[90:91] neg_lo:[0,1] neg_hi:[0,1]
	v_min_f32_e32 v90, 0, v92
	v_add_f32_e32 v91, v17, v97
	v_mul_f32_e64 v92, |v91|, s35
	v_exp_f32_e32 v120, v92
	v_min_f32_e32 v91, 0, v91
	s_nop 15
	s_nop 3
	v_mfma_f32_16x16x32_bf16 v[94:97], v[22:25], v[66:69], 0
	s_nop 13
	v_add_f32_e32 v93, 1.0, v120
	v_log_f32_e32 v93, v93
	s_nop 1
	v_mul_f32_e32 v93, 0x3f317218, v93
	s_nop 5
	v_add_f32_e32 v92, 1.0, v121
	v_log_f32_e32 v92, v92
	s_nop 1
	v_mul_f32_e32 v92, 0x3f317218, v92
	s_nop 1
	v_pk_add_f32 v[90:91], v[90:91], v[92:93] neg_lo:[0,1] neg_hi:[0,1]
	v_add_f32_e32 v89, v26, v94
	v_pk_mul_f32 v[92:93], v[90:91], s[44:45] op_sel_hi:[1,0]
	v_pk_mul_f32 v[90:91], v[82:83], s[44:45] op_sel_hi:[1,0]
	v_mul_f32_e64 v82, |v89|, s35
	v_exp_f32_e32 v120, v82
	v_lshl_add_u64 v[82:83], s[10:11], 2, v[70:71]
	global_store_dwordx4 v[82:83], v[90:93], off
	v_min_f32_e32 v82, 0, v89
	v_add_f32_e32 v83, v27, v95
	v_mul_f32_e64 v90, |v83|, s35
	v_exp_f32_e32 v121, v90
	v_min_f32_e32 v83, 0, v83
	s_nop 15
	s_nop 3
	v_add_f32_e32 v92, v28, v96
	s_nop 13
	v_add_f32_e32 v91, 1.0, v121
	v_log_f32_e32 v91, v91
	s_nop 1
	v_mul_f32_e32 v91, 0x3f317218, v91
	s_nop 1
	v_mul_f32_e64 v90, |v92|, s35
	v_exp_f32_e32 v121, v90
	s_nop 3
	v_add_f32_e32 v90, 1.0, v120
	v_log_f32_e32 v90, v90
	s_nop 1
	v_mul_f32_e32 v90, 0x3f317218, v90
	s_nop 1
	v_pk_add_f32 v[82:83], v[82:83], v[90:91] neg_lo:[0,1] neg_hi:[0,1]
	v_min_f32_e32 v90, 0, v92
	v_add_f32_e32 v91, v29, v97
	v_mul_f32_e64 v92, |v91|, s35
	v_exp_f32_e32 v120, v92
	v_min_f32_e32 v91, 0, v91
	s_nop 15
	s_nop 3
	v_mfma_f32_16x16x32_bf16 v[94:97], v[18:21], v[66:69], 0
	s_nop 13
	v_add_f32_e32 v93, 1.0, v120
	v_log_f32_e32 v93, v93
	s_nop 1
	v_mul_f32_e32 v93, 0x3f317218, v93
	s_nop 5
	v_add_f32_e32 v92, 1.0, v121
	v_log_f32_e32 v92, v92
	s_nop 1
	v_mul_f32_e32 v92, 0x3f317218, v92
	s_nop 1
	v_pk_add_f32 v[90:91], v[90:91], v[92:93] neg_lo:[0,1] neg_hi:[0,1]
	v_add_f32_e32 v89, v30, v94
	v_pk_mul_f32 v[92:93], v[90:91], s[44:45] op_sel_hi:[1,0]
	v_pk_mul_f32 v[90:91], v[82:83], s[44:45] op_sel_hi:[1,0]
	v_mul_f32_e64 v82, |v89|, s35
	v_exp_f32_e32 v120, v82
	v_lshl_add_u64 v[82:83], s[12:13], 2, v[70:71]
	global_store_dwordx4 v[82:83], v[90:93], off
	v_min_f32_e32 v82, 0, v89
	v_add_f32_e32 v83, v31, v95
	v_mul_f32_e64 v90, |v83|, s35
	v_exp_f32_e32 v121, v90
	v_min_f32_e32 v83, 0, v83
	s_nop 15
	s_nop 3
	v_add_f32_e32 v92, v32, v96
	s_nop 13
	v_add_f32_e32 v91, 1.0, v121
	v_log_f32_e32 v91, v91
	s_nop 1
	v_mul_f32_e32 v91, 0x3f317218, v91
	s_nop 1
	v_mul_f32_e64 v90, |v92|, s35
	v_exp_f32_e32 v121, v90
	s_nop 3
	v_add_f32_e32 v90, 1.0, v120
	v_log_f32_e32 v90, v90
	s_nop 1
	v_mul_f32_e32 v90, 0x3f317218, v90
	s_nop 1
	v_pk_add_f32 v[82:83], v[82:83], v[90:91] neg_lo:[0,1] neg_hi:[0,1]
	v_min_f32_e32 v90, 0, v92
	v_add_f32_e32 v91, v33, v97
	v_mul_f32_e64 v92, |v91|, s35
	v_exp_f32_e32 v120, v92
	v_min_f32_e32 v91, 0, v91
	s_nop 15
	s_nop 3
	v_mfma_f32_16x16x32_bf16 v[94:97], v[38:41], v[66:69], 0
	s_nop 13
	v_add_f32_e32 v93, 1.0, v120
	v_log_f32_e32 v93, v93
	s_nop 1
	v_mul_f32_e32 v93, 0x3f317218, v93
	s_nop 5
	v_add_f32_e32 v92, 1.0, v121
	v_log_f32_e32 v92, v92
	s_nop 1
	v_mul_f32_e32 v92, 0x3f317218, v92
	s_nop 1
	v_pk_add_f32 v[90:91], v[90:91], v[92:93] neg_lo:[0,1] neg_hi:[0,1]
	v_add_f32_e32 v89, v42, v94
	v_pk_mul_f32 v[92:93], v[90:91], s[44:45] op_sel_hi:[1,0]
	v_pk_mul_f32 v[90:91], v[82:83], s[44:45] op_sel_hi:[1,0]
	v_mul_f32_e64 v82, |v89|, s35
	v_exp_f32_e32 v120, v82
	v_lshl_add_u64 v[82:83], s[14:15], 2, v[70:71]
	global_store_dwordx4 v[82:83], v[90:93], off
	v_min_f32_e32 v82, 0, v89
	v_add_f32_e32 v83, v43, v95
	v_mul_f32_e64 v90, |v83|, s35
	v_exp_f32_e32 v121, v90
	v_min_f32_e32 v83, 0, v83
	s_nop 15
	s_nop 3
	v_add_f32_e32 v92, v44, v96
	s_nop 13
	v_add_f32_e32 v91, 1.0, v121
	v_log_f32_e32 v91, v91
	s_nop 1
	v_mul_f32_e32 v91, 0x3f317218, v91
	s_nop 1
	v_mul_f32_e64 v90, |v92|, s35
	v_exp_f32_e32 v121, v90
	s_nop 3
	v_add_f32_e32 v90, 1.0, v120
	v_log_f32_e32 v90, v90
	s_nop 1
	v_mul_f32_e32 v90, 0x3f317218, v90
	s_nop 1
	v_pk_add_f32 v[82:83], v[82:83], v[90:91] neg_lo:[0,1] neg_hi:[0,1]
	v_min_f32_e32 v90, 0, v92
	v_add_f32_e32 v91, v45, v97
	v_mul_f32_e64 v92, |v91|, s35
	v_exp_f32_e32 v120, v92
	v_min_f32_e32 v91, 0, v91
	s_nop 15
	s_nop 3
	v_mfma_f32_16x16x32_bf16 v[94:97], v[34:37], v[66:69], 0
	s_nop 13
	v_add_f32_e32 v93, 1.0, v120
	v_log_f32_e32 v93, v93
	s_nop 1
	v_mul_f32_e32 v93, 0x3f317218, v93
	s_nop 5
	v_add_f32_e32 v92, 1.0, v121
	v_log_f32_e32 v92, v92
	s_nop 1
	v_mul_f32_e32 v92, 0x3f317218, v92
	s_nop 1
	v_pk_add_f32 v[90:91], v[90:91], v[92:93] neg_lo:[0,1] neg_hi:[0,1]
	v_add_f32_e32 v89, v46, v94
	v_pk_mul_f32 v[92:93], v[90:91], s[44:45] op_sel_hi:[1,0]
	v_pk_mul_f32 v[90:91], v[82:83], s[44:45] op_sel_hi:[1,0]
	v_mul_f32_e64 v82, |v89|, s35
	v_exp_f32_e32 v120, v82
	v_lshl_add_u64 v[82:83], s[16:17], 2, v[70:71]
	global_store_dwordx4 v[82:83], v[90:93], off
	v_min_f32_e32 v82, 0, v89
	v_add_f32_e32 v83, v47, v95
	v_mul_f32_e64 v90, |v83|, s35
	v_exp_f32_e32 v121, v90
	v_min_f32_e32 v83, 0, v83
	s_nop 15
	s_nop 3
	v_add_f32_e32 v92, v48, v96
	s_nop 13
	v_add_f32_e32 v91, 1.0, v121
	v_log_f32_e32 v91, v91
	s_nop 1
	v_mul_f32_e32 v91, 0x3f317218, v91
	s_nop 1
	v_mul_f32_e64 v90, |v92|, s35
	v_exp_f32_e32 v121, v90
	s_nop 3
	v_add_f32_e32 v90, 1.0, v120
	v_log_f32_e32 v90, v90
	s_nop 1
	v_mul_f32_e32 v90, 0x3f317218, v90
	s_nop 1
	v_pk_add_f32 v[82:83], v[82:83], v[90:91] neg_lo:[0,1] neg_hi:[0,1]
	v_min_f32_e32 v90, 0, v92
	v_add_f32_e32 v91, v49, v97
	v_mul_f32_e64 v92, |v91|, s35
	v_exp_f32_e32 v120, v92
	v_min_f32_e32 v91, 0, v91
	s_nop 15
	s_nop 3
	v_mfma_f32_16x16x32_bf16 v[94:97], v[54:57], v[66:69], 0
	v_mfma_f32_16x16x32_bf16 v[66:69], v[50:53], v[66:69], 0
	s_nop 7
	v_add_f32_e32 v66, v62, v66
	v_add_f32_e32 v67, v63, v67
	v_add_f32_e32 v68, v64, v68
	v_add_f32_e32 v69, v65, v69
	s_nop 5
	v_add_f32_e32 v93, 1.0, v120
	v_log_f32_e32 v93, v93
	s_nop 1
	v_mul_f32_e32 v93, 0x3f317218, v93
	s_nop 5
	v_add_f32_e32 v92, 1.0, v121
	v_log_f32_e32 v92, v92
	s_nop 1
	v_mul_f32_e32 v92, 0x3f317218, v92
	s_nop 1
	v_pk_add_f32 v[90:91], v[90:91], v[92:93] neg_lo:[0,1] neg_hi:[0,1]
	v_add_f32_e32 v89, v58, v94
	v_pk_mul_f32 v[92:93], v[90:91], s[44:45] op_sel_hi:[1,0]
	v_pk_mul_f32 v[90:91], v[82:83], s[44:45] op_sel_hi:[1,0]
	v_mul_f32_e64 v82, |v89|, s35
	v_exp_f32_e32 v120, v82
	v_lshl_add_u64 v[82:83], s[18:19], 2, v[70:71]
	global_store_dwordx4 v[82:83], v[90:93], off
	v_min_f32_e32 v82, 0, v89
	v_add_f32_e32 v83, v59, v95
	v_mul_f32_e64 v90, |v83|, s35
	v_exp_f32_e32 v121, v90
	v_min_f32_e32 v83, 0, v83
	s_nop 15
	s_nop 3
	v_add_f32_e32 v92, v60, v96
	s_nop 13
	v_add_f32_e32 v91, 1.0, v121
	v_log_f32_e32 v91, v91
	s_nop 1
	v_mul_f32_e32 v91, 0x3f317218, v91
	s_nop 1
	v_mul_f32_e64 v90, |v92|, s35
	v_exp_f32_e32 v121, v90
	s_nop 3
	v_add_f32_e32 v90, 1.0, v120
	v_log_f32_e32 v90, v90
	s_nop 1
	v_mul_f32_e32 v90, 0x3f317218, v90
	s_nop 1
	v_pk_add_f32 v[82:83], v[82:83], v[90:91] neg_lo:[0,1] neg_hi:[0,1]
	v_min_f32_e32 v90, 0, v92
	v_add_f32_e32 v91, v61, v97
	v_mul_f32_e64 v92, |v91|, s35
	v_exp_f32_e32 v120, v92
	v_min_f32_e32 v91, 0, v91
	s_nop 15
	s_nop 15
	s_nop 2
	v_add_f32_e32 v93, 1.0, v120
	v_log_f32_e32 v93, v93
	s_nop 1
	v_mul_f32_e32 v93, 0x3f317218, v93
	s_nop 5
	v_add_f32_e32 v92, 1.0, v121
	v_log_f32_e32 v92, v92
	s_nop 1
	v_mul_f32_e32 v92, 0x3f317218, v92
	s_nop 1
	v_pk_add_f32 v[90:91], v[90:91], v[92:93] neg_lo:[0,1] neg_hi:[0,1]
	s_nop 0
	v_pk_mul_f32 v[92:93], v[90:91], s[44:45] op_sel_hi:[1,0]
	v_pk_mul_f32 v[90:91], v[82:83], s[44:45] op_sel_hi:[1,0]
	v_mul_f32_e64 v82, |v66|, s35
	v_exp_f32_e32 v89, v82
	v_lshl_add_u64 v[82:83], s[20:21], 2, v[70:71]
	global_store_dwordx4 v[82:83], v[90:93], off
	v_min_f32_e32 v66, 0, v66
	v_lshl_add_u64 v[70:71], s[22:23], 2, v[70:71]
	v_mul_f32_e64 v82, |v67|, s35
	v_exp_f32_e32 v116, v82
	v_min_f32_e32 v67, 0, v67
	s_nop 15
	s_nop 3
	v_mul_f32_e64 v90, |v68|, s35
	v_min_f32_e32 v68, 0, v68
	s_nop 12
	v_add_f32_e32 v83, 1.0, v116
	v_log_f32_e32 v83, v83
	s_nop 1
	v_mul_f32_e32 v83, 0x3f317218, v83
	s_nop 1
	v_exp_f32_e32 v116, v90
	s_nop 3
	v_add_f32_e32 v82, 1.0, v89
	v_log_f32_e32 v82, v82
	s_nop 1
	v_mul_f32_e32 v82, 0x3f317218, v82
	s_nop 1
	v_pk_add_f32 v[66:67], v[66:67], v[82:83] neg_lo:[0,1] neg_hi:[0,1]
	v_mul_f32_e64 v82, |v69|, s35
	v_exp_f32_e32 v117, v82
	v_min_f32_e32 v69, 0, v69
	v_pk_mul_f32 v[66:67], v[66:67], s[44:45] op_sel_hi:[1,0]
	s_nop 15
	s_nop 15
	s_nop 2
	v_add_f32_e32 v81, 1.0, v117
	v_log_f32_e32 v81, v81
	s_nop 1
	v_mul_f32_e32 v81, 0x3f317218, v81
	s_nop 5
	v_add_f32_e32 v80, 1.0, v116
	v_log_f32_e32 v80, v80
	s_nop 1
	v_mul_f32_e32 v80, 0x3f317218, v80
	s_nop 1
	v_pk_add_f32 v[68:69], v[68:69], v[80:81] neg_lo:[0,1] neg_hi:[0,1]
	s_nop 0
	v_pk_mul_f32 v[68:69], v[68:69], s[44:45] op_sel_hi:[1,0]
	global_store_dwordx4 v[70:71], v[66:69], off
	v_mov_b32_e32 v70, 0
	v_mov_b32_e32 v71, 0
	v_mov_b32_e32 v66, 0
	v_mov_b32_e32 v68, 0
	v_mov_b32_e32 v69, 0
	s_and_saveexec_b64 s[72:73], s[4:5]
	ds_read_b128 v[68:71], v72 offset:1024
	s_or_b64 exec, exec, s[72:73]
	s_waitcnt lgkmcnt(0)
	v_mfma_f32_16x16x32_bf16 v[90:93], v[6:9], v[68:71], 0
	v_lshl_add_u64 v[80:81], v[78:79], 0, s[64:65]
	s_nop 6
	v_add_f32_e32 v67, v10, v90
	v_mul_f32_e64 v82, |v67|, s35
	v_exp_f32_e32 v89, v82
	v_add_f32_e32 v91, v11, v91
	v_min_f32_e32 v90, 0, v67
	v_mul_f32_e64 v67, |v91|, s35
	v_exp_f32_e32 v67, v67
	v_min_f32_e32 v91, 0, v91
	v_add_f32_e32 v93, v13, v93
	s_nop 15
	s_nop 15
	s_nop 1
	v_add_f32_e32 v95, 1.0, v67
	v_log_f32_e32 v95, v95
	s_nop 1
	v_mul_f32_e32 v95, 0x3f317218, v95
	s_nop 1
	v_add_f32_e32 v67, v12, v92
	v_mul_f32_e64 v92, |v67|, s35
	v_exp_f32_e32 v122, v92
	v_min_f32_e32 v92, 0, v67
	s_nop 1
	v_add_f32_e32 v94, 1.0, v89
	v_log_f32_e32 v94, v94
	s_nop 1
	v_mul_f32_e32 v94, 0x3f317218, v94
	s_nop 1
	v_pk_add_f32 v[90:91], v[90:91], v[94:95] neg_lo:[0,1] neg_hi:[0,1]
	v_mul_f32_e64 v94, |v93|, s35
	v_exp_f32_e32 v123, v94
	v_min_f32_e32 v93, 0, v93
	v_pk_mul_f32 v[90:91], v[90:91], s[44:45] op_sel_hi:[1,0]
	s_nop 15
	s_nop 1
	v_lshl_add_u64 v[98:99], s[2:3], 2, v[80:81]
	s_nop 14
	v_add_f32_e32 v95, 1.0, v123
	v_log_f32_e32 v95, v95
	s_nop 1
	v_mul_f32_e32 v95, 0x3f317218, v95
	s_nop 5
	v_add_f32_e32 v94, 1.0, v122
	v_log_f32_e32 v94, v94
	s_nop 1
	v_mul_f32_e32 v94, 0x3f317218, v94
	s_nop 1
	v_pk_add_f32 v[92:93], v[92:93], v[94:95] neg_lo:[0,1] neg_hi:[0,1]
	v_mfma_f32_16x16x32_bf16 v[94:97], v[2:5], v[68:71], 0
	v_mul_f32_e64 v92, v92, s44
	v_mul_f32_e64 v93, v93, s44
	global_store_dwordx4 v[98:99], v[90:93], off
	s_nop 4
	v_add_f32_e32 v67, v14, v94
	v_mul_f32_e64 v89, |v67|, s35
	v_exp_f32_e32 v89, v89
	v_min_f32_e32 v90, 0, v67
	v_add_f32_e32 v91, v15, v95
	v_mul_f32_e64 v92, |v91|, s35
	v_exp_f32_e32 v122, v92
	v_min_f32_e32 v91, 0, v91
	s_nop 15
	s_nop 3
	v_add_f32_e32 v94, v16, v96
	s_nop 13
	v_add_f32_e32 v93, 1.0, v122
	v_log_f32_e32 v93, v93
	s_nop 1
	v_mul_f32_e32 v93, 0x3f317218, v93
	s_nop 1
	v_mul_f32_e64 v92, |v94|, s35
	v_exp_f32_e32 v122, v92
	s_nop 3
	v_add_f32_e32 v92, 1.0, v89
	v_log_f32_e32 v92, v92
	s_nop 1
	v_mul_f32_e32 v92, 0x3f317218, v92
	s_nop 1
	v_pk_add_f32 v[90:91], v[90:91], v[92:93] neg_lo:[0,1] neg_hi:[0,1]
	v_add_f32_e32 v93, v17, v97
	v_min_f32_e32 v92, 0, v94
	v_mul_f32_e64 v94, |v93|, s35
	v_exp_f32_e32 v123, v94
	v_min_f32_e32 v93, 0, v93
	v_pk_mul_f32 v[90:91], v[90:91], s[44:45] op_sel_hi:[1,0]
	s_nop 15
	s_nop 1
	v_lshl_add_u64 v[98:99], s[10:11], 2, v[80:81]
	s_nop 14
	v_add_f32_e32 v95, 1.0, v123
	v_log_f32_e32 v95, v95
	s_nop 1
	v_mul_f32_e32 v95, 0x3f317218, v95
	s_nop 5
	v_add_f32_e32 v94, 1.0, v122
	v_log_f32_e32 v94, v94
	s_nop 1
	v_mul_f32_e32 v94, 0x3f317218, v94
	s_nop 1
	v_pk_add_f32 v[92:93], v[92:93], v[94:95] neg_lo:[0,1] neg_hi:[0,1]
	v_mfma_f32_16x16x32_bf16 v[94:97], v[22:25], v[68:71], 0
	v_mul_f32_e64 v92, v92, s44
	v_mul_f32_e64 v93, v93, s44
	global_store_dwordx4 v[98:99], v[90:93], off
	s_nop 4
	v_add_f32_e32 v67, v26, v94
	v_mul_f32_e64 v89, |v67|, s35
	v_exp_f32_e32 v89, v89
	v_min_f32_e32 v90, 0, v67
	v_add_f32_e32 v91, v27, v95
	v_mul_f32_e64 v92, |v91|, s35
	v_exp_f32_e32 v122, v92
	v_min_f32_e32 v91, 0, v91
	s_nop 15
	s_nop 3
	v_add_f32_e32 v94, v28, v96
	s_nop 13
	v_add_f32_e32 v93, 1.0, v122
	v_log_f32_e32 v93, v93
	s_nop 1
	v_mul_f32_e32 v93, 0x3f317218, v93
	s_nop 1
	v_mul_f32_e64 v92, |v94|, s35
	v_exp_f32_e32 v122, v92
	s_nop 3
	v_add_f32_e32 v92, 1.0, v89
	v_log_f32_e32 v92, v92
	s_nop 1
	v_mul_f32_e32 v92, 0x3f317218, v92
	s_nop 1
	v_pk_add_f32 v[90:91], v[90:91], v[92:93] neg_lo:[0,1] neg_hi:[0,1]
	v_add_f32_e32 v93, v29, v97
	v_min_f32_e32 v92, 0, v94
	v_mul_f32_e64 v94, |v93|, s35
	v_exp_f32_e32 v123, v94
	v_min_f32_e32 v93, 0, v93
	v_pk_mul_f32 v[90:91], v[90:91], s[44:45] op_sel_hi:[1,0]
	s_nop 15
	s_nop 1
	v_lshl_add_u64 v[98:99], s[12:13], 2, v[80:81]
	s_nop 14
	v_add_f32_e32 v95, 1.0, v123
	v_log_f32_e32 v95, v95
	s_nop 1
	v_mul_f32_e32 v95, 0x3f317218, v95
	s_nop 5
	v_add_f32_e32 v94, 1.0, v122
	v_log_f32_e32 v94, v94
	s_nop 1
	v_mul_f32_e32 v94, 0x3f317218, v94
	s_nop 1
	v_pk_add_f32 v[92:93], v[92:93], v[94:95] neg_lo:[0,1] neg_hi:[0,1]
	v_mfma_f32_16x16x32_bf16 v[94:97], v[18:21], v[68:71], 0
	v_mul_f32_e64 v92, v92, s44
	v_mul_f32_e64 v93, v93, s44
	global_store_dwordx4 v[98:99], v[90:93], off
	s_nop 4
	v_add_f32_e32 v67, v30, v94
	v_mul_f32_e64 v89, |v67|, s35
	v_exp_f32_e32 v89, v89
	v_min_f32_e32 v90, 0, v67
	v_add_f32_e32 v91, v31, v95
	v_mul_f32_e64 v92, |v91|, s35
	v_exp_f32_e32 v122, v92
	v_min_f32_e32 v91, 0, v91
	s_nop 15
	s_nop 3
	v_add_f32_e32 v94, v32, v96
	s_nop 13
	v_add_f32_e32 v93, 1.0, v122
	v_log_f32_e32 v93, v93
	s_nop 1
	v_mul_f32_e32 v93, 0x3f317218, v93
	s_nop 1
	v_mul_f32_e64 v92, |v94|, s35
	v_exp_f32_e32 v122, v92
	s_nop 3
	v_add_f32_e32 v92, 1.0, v89
	v_log_f32_e32 v92, v92
	s_nop 1
	v_mul_f32_e32 v92, 0x3f317218, v92
	s_nop 1
	v_pk_add_f32 v[90:91], v[90:91], v[92:93] neg_lo:[0,1] neg_hi:[0,1]
	v_add_f32_e32 v93, v33, v97
	v_min_f32_e32 v92, 0, v94
	v_mul_f32_e64 v94, |v93|, s35
	v_exp_f32_e32 v123, v94
	v_min_f32_e32 v93, 0, v93
	v_pk_mul_f32 v[90:91], v[90:91], s[44:45] op_sel_hi:[1,0]
	s_nop 15
	s_nop 1
	v_lshl_add_u64 v[98:99], s[14:15], 2, v[80:81]
	s_nop 14
	v_add_f32_e32 v95, 1.0, v123
	v_log_f32_e32 v95, v95
	s_nop 1
	v_mul_f32_e32 v95, 0x3f317218, v95
	s_nop 5
	v_add_f32_e32 v94, 1.0, v122
	v_log_f32_e32 v94, v94
	s_nop 1
	v_mul_f32_e32 v94, 0x3f317218, v94
	s_nop 1
	v_pk_add_f32 v[92:93], v[92:93], v[94:95] neg_lo:[0,1] neg_hi:[0,1]
	v_mfma_f32_16x16x32_bf16 v[94:97], v[38:41], v[68:71], 0
	v_mul_f32_e64 v92, v92, s44
	v_mul_f32_e64 v93, v93, s44
	global_store_dwordx4 v[98:99], v[90:93], off
	s_nop 4
	v_add_f32_e32 v67, v42, v94
	v_mul_f32_e64 v89, |v67|, s35
	v_exp_f32_e32 v89, v89
	v_min_f32_e32 v90, 0, v67
	v_add_f32_e32 v91, v43, v95
	v_mul_f32_e64 v92, |v91|, s35
	v_exp_f32_e32 v122, v92
	v_min_f32_e32 v91, 0, v91
	s_nop 15
	s_nop 3
	v_add_f32_e32 v94, v44, v96
	s_nop 13
	v_add_f32_e32 v93, 1.0, v122
	v_log_f32_e32 v93, v93
	s_nop 1
	v_mul_f32_e32 v93, 0x3f317218, v93
	s_nop 1
	v_mul_f32_e64 v92, |v94|, s35
	v_exp_f32_e32 v122, v92
	s_nop 3
	v_add_f32_e32 v92, 1.0, v89
	v_log_f32_e32 v92, v92
	s_nop 1
	v_mul_f32_e32 v92, 0x3f317218, v92
	s_nop 1
	v_pk_add_f32 v[90:91], v[90:91], v[92:93] neg_lo:[0,1] neg_hi:[0,1]
	v_add_f32_e32 v93, v45, v97
	v_min_f32_e32 v92, 0, v94
	v_mul_f32_e64 v94, |v93|, s35
	v_exp_f32_e32 v123, v94
	v_min_f32_e32 v93, 0, v93
	v_pk_mul_f32 v[90:91], v[90:91], s[44:45] op_sel_hi:[1,0]
	s_nop 15
	s_nop 1
	v_lshl_add_u64 v[98:99], s[16:17], 2, v[80:81]
	s_nop 14
	v_add_f32_e32 v95, 1.0, v123
	v_log_f32_e32 v95, v95
	s_nop 1
	v_mul_f32_e32 v95, 0x3f317218, v95
	s_nop 5
	v_add_f32_e32 v94, 1.0, v122
	v_log_f32_e32 v94, v94
	s_nop 1
	v_mul_f32_e32 v94, 0x3f317218, v94
	s_nop 1
	v_pk_add_f32 v[92:93], v[92:93], v[94:95] neg_lo:[0,1] neg_hi:[0,1]
	v_mfma_f32_16x16x32_bf16 v[94:97], v[34:37], v[68:71], 0
	v_mul_f32_e64 v92, v92, s44
	v_mul_f32_e64 v93, v93, s44
	global_store_dwordx4 v[98:99], v[90:93], off
	s_nop 4
	v_add_f32_e32 v67, v46, v94
	v_mul_f32_e64 v89, |v67|, s35
	v_exp_f32_e32 v89, v89
	v_min_f32_e32 v90, 0, v67
	v_add_f32_e32 v91, v47, v95
	v_mul_f32_e64 v92, |v91|, s35
	v_exp_f32_e32 v122, v92
	v_min_f32_e32 v91, 0, v91
	s_nop 15
	s_nop 3
	v_add_f32_e32 v94, v48, v96
	s_nop 13
	v_add_f32_e32 v93, 1.0, v122
	v_log_f32_e32 v93, v93
	s_nop 1
	v_mul_f32_e32 v93, 0x3f317218, v93
	s_nop 1
	v_mul_f32_e64 v92, |v94|, s35
	v_exp_f32_e32 v122, v92
	s_nop 3
	v_add_f32_e32 v92, 1.0, v89
	v_log_f32_e32 v92, v92
	s_nop 1
	v_mul_f32_e32 v92, 0x3f317218, v92
	s_nop 1
	v_pk_add_f32 v[90:91], v[90:91], v[92:93] neg_lo:[0,1] neg_hi:[0,1]
	v_add_f32_e32 v93, v49, v97
	v_min_f32_e32 v92, 0, v94
	v_mul_f32_e64 v94, |v93|, s35
	v_exp_f32_e32 v123, v94
	v_min_f32_e32 v93, 0, v93
	v_pk_mul_f32 v[90:91], v[90:91], s[44:45] op_sel_hi:[1,0]
	s_nop 15
	s_nop 1
	v_lshl_add_u64 v[98:99], s[18:19], 2, v[80:81]
	s_nop 14
	v_add_f32_e32 v95, 1.0, v123
	v_log_f32_e32 v95, v95
	s_nop 1
	v_mul_f32_e32 v95, 0x3f317218, v95
	s_nop 5
	v_add_f32_e32 v94, 1.0, v122
	v_log_f32_e32 v94, v94
	s_nop 1
	v_mul_f32_e32 v94, 0x3f317218, v94
	s_nop 1
	v_pk_add_f32 v[92:93], v[92:93], v[94:95] neg_lo:[0,1] neg_hi:[0,1]
	v_mfma_f32_16x16x32_bf16 v[94:97], v[54:57], v[68:71], 0
	v_mul_f32_e64 v92, v92, s44
	v_mul_f32_e64 v93, v93, s44
	global_store_dwordx4 v[98:99], v[90:93], off
	v_mfma_f32_16x16x32_bf16 v[68:71], v[50:53], v[68:71], 0
	s_nop 3
	v_add_f32_e32 v67, v58, v94
	v_mul_f32_e64 v89, |v67|, s35
	v_exp_f32_e32 v89, v89
	v_min_f32_e32 v90, 0, v67
	v_add_f32_e32 v69, v63, v69
	v_add_f32_e32 v70, v64, v70
	v_add_f32_e32 v91, v59, v95
	v_mul_f32_e64 v92, |v91|, s35
	v_exp_f32_e32 v122, v92
	v_min_f32_e32 v91, 0, v91
	v_add_f32_e32 v71, v65, v71
	s_nop 15
	s_nop 2
	v_add_f32_e32 v94, v60, v96
	s_nop 13
	v_add_f32_e32 v93, 1.0, v122
	v_log_f32_e32 v93, v93
	s_nop 1
	v_mul_f32_e32 v93, 0x3f317218, v93
	s_nop 1
	v_mul_f32_e64 v92, |v94|, s35
	v_exp_f32_e32 v122, v92
	s_nop 3
	v_add_f32_e32 v92, 1.0, v89
	v_log_f32_e32 v92, v92
	s_nop 1
	v_mul_f32_e32 v92, 0x3f317218, v92
	s_nop 1
	v_pk_add_f32 v[90:91], v[90:91], v[92:93] neg_lo:[0,1] neg_hi:[0,1]
	v_add_f32_e32 v93, v61, v97
	v_min_f32_e32 v92, 0, v94
	v_mul_f32_e64 v94, |v93|, s35
	v_exp_f32_e32 v123, v94
	v_min_f32_e32 v93, 0, v93
	v_pk_mul_f32 v[90:91], v[90:91], s[44:45] op_sel_hi:[1,0]
	s_nop 15
	s_nop 15
	s_nop 1
	v_add_f32_e32 v95, 1.0, v123
	v_log_f32_e32 v95, v95
	s_nop 1
	v_mul_f32_e32 v95, 0x3f317218, v95
	s_nop 5
	v_add_f32_e32 v94, 1.0, v122
	v_log_f32_e32 v94, v94
	s_nop 1
	v_mul_f32_e32 v94, 0x3f317218, v94
	s_nop 1
	v_add_f32_e32 v67, v62, v68
	v_mul_f32_e64 v68, |v67|, s35
	v_exp_f32_e32 v89, v68
	v_pk_add_f32 v[92:93], v[92:93], v[94:95] neg_lo:[0,1] neg_hi:[0,1]
	v_lshl_add_u64 v[94:95], s[20:21], 2, v[80:81]
	v_pk_mul_f32 v[92:93], v[92:93], s[44:45] op_sel_hi:[1,0]
	v_min_f32_e32 v68, 0, v67
	global_store_dwordx4 v[94:95], v[90:93], off
	v_lshl_add_u64 v[80:81], s[22:23], 2, v[80:81]
	s_nop 0
	v_mul_f32_e64 v90, |v69|, s35
	v_exp_f32_e32 v118, v90
	v_min_f32_e32 v69, 0, v69
	s_nop 15
	s_nop 15
	s_nop 2
	v_add_f32_e32 v91, 1.0, v118
	v_log_f32_e32 v91, v91
	s_nop 1
	v_mul_f32_e32 v91, 0x3f317218, v91
	s_nop 1
	v_mul_f32_e64 v90, |v70|, s35
	v_exp_f32_e32 v118, v90
	v_min_f32_e32 v70, 0, v70
	s_nop 2
	v_add_f32_e32 v90, 1.0, v89
	v_log_f32_e32 v90, v90
	s_nop 1
	v_mul_f32_e32 v90, 0x3f317218, v90
	s_nop 1
	v_pk_add_f32 v[68:69], v[68:69], v[90:91] neg_lo:[0,1] neg_hi:[0,1]
	v_mul_f32_e64 v90, |v71|, s35
	v_exp_f32_e32 v119, v90
	v_min_f32_e32 v71, 0, v71
	v_pk_mul_f32 v[68:69], v[68:69], s[44:45] op_sel_hi:[1,0]
	s_nop 15
	s_nop 15
	s_nop 2
	v_add_f32_e32 v83, 1.0, v119
	v_log_f32_e32 v83, v83
	s_nop 1
	v_mul_f32_e32 v83, 0x3f317218, v83
	s_nop 1
	v_cmp_lt_f32_e64 vcc, |v118|, s45
	s_nop 3
	v_add_f32_e32 v82, 1.0, v118
	v_log_f32_e32 v82, v82
	s_nop 1
	v_mul_f32_e32 v82, 0x3f317218, v82
	s_nop 1
	v_pk_add_f32 v[70:71], v[70:71], v[82:83] neg_lo:[0,1] neg_hi:[0,1]
	v_mov_b32_e32 v67, 0
	v_pk_mul_f32 v[70:71], v[70:71], s[44:45] op_sel_hi:[1,0]
	global_store_dwordx4 v[80:81], v[68:71], off
	s_nop 1
	v_mov_b32_e32 v68, 0
	v_mov_b32_e32 v69, 0
	s_and_saveexec_b64 s[72:73], s[4:5]
	s_cbranch_execz .LBB0_146
	ds_read_b128 v[66:69], v72 offset:1536
	s_branch .LBB0_146
